# attention units split 1056 / 480 between the scan phase's spare workgroups and the mixer-prep phase
# baseline (speedup 1.0000x reference)
; #define LAS __attribute__((address_space(3)))
; DI void attn_unit(const Args& A, LAS unsigned char* lds, int unit, int tid, int wave, int lane) {
;     const bf16* Z = (const bf16*)(A.ws + WS_Z); bf16* ao = (bf16*)(A.ws + WS_ATTO); float* al = (float*)(A.ws + WS_ATTL);
;     const int x = unit & 15; int r0 = unit >> 4; const int hh = r0 & 3; r0 >>= 2; const int b = r0 % NB, br = r0 / NB;
;     const int dil = br == 0 ? 1 : (br == 1 ? 4 : 16), lsub = SEQ / dil, nblk = lsub / 128;
;     const int res = x / nblk, nbk = x % nblk, l0 = nbk * 128, wbase = l0 - 64;
;     LAS bf16* Qs = (LAS bf16*)(lds + AT_QS); LAS bf16* Ks = (LAS bf16*)(lds + AT_KS); LAS bf16* Vt = (LAS bf16*)(lds + AT_VT); LAS float* btab = (LAS float*)(lds + AT_BT);
;     __syncthreads();
; #pragma unroll
;     for (int i = 0; i < 2; ++i) { const int id = tid + 512 * i, row = id >> 3, ch = id & 7; const int tok = b * SEQ + (l0 + row) * dil + res;
;         *(LAS u32x4_t*)(Qs + row * AT_QLD + ch * 8) = *(const u32x4_t*)(Z + (size_t)tok * ZLD + ZA + hh * 64 + ch * 8); }
;     for (int id = tid; id < 272 * 8; id += NTHR) { const int row = id >> 3, ch = id & 7; const int pos = wbase + row; u32x4_t v = (u32x4_t){0u, 0u, 0u, 0u};
;         if (row < 256 && pos >= 0 && pos < lsub) v = *(const u32x4_t*)(Z + (size_t)(b * SEQ + pos * dil + res) * ZLD + ZA + 256 + hh * 64 + ch * 8);
;         *(LAS u32x4_t*)(Ks + row * AT_QLD + ch * 8) = v; }
;     for (int id = tid; id < 272 * 8; id += NTHR) { const int key = id % 272, ch = id / 272; const int pos = wbase + key; u32x4_t v = (u32x4_t){0u, 0u, 0u, 0u};
;         if (key < 256 && pos >= 0 && pos < lsub) v = *(const u32x4_t*)(Z + (size_t)(b * SEQ + pos * dil + res) * ZLD + ZA + 512 + hh * 64 + ch * 8);
;         LAS bf16* d = Vt + (ch * 8) * AT_VLD + key;
;         d[0] = (bf16)(v.x & 0xffffu); d[AT_VLD] = (bf16)(v.x >> 16); d[2 * AT_VLD] = (bf16)(v.y & 0xffffu); d[3 * AT_VLD] = (bf16)(v.y >> 16);
;         d[4 * AT_VLD] = (bf16)(v.z & 0xffffu); d[5 * AT_VLD] = (bf16)(v.z >> 16); d[6 * AT_VLD] = (bf16)(v.w & 0xffffu); d[7 * AT_VLD] = (bf16)(v.w >> 16); }
;     if (tid < 129) btab[tid] = A.in[I_RELB][t5_bucket((tid - 64) * dil) * 4 + hh] * 1.4426950408889634f;
;     __syncthreads();
.LBB0_244:
	s_cmp_lt_i32 s6, 4
	s_cselect_b64 s[0:1], -1, 0
	v_writelane_b32 v235, s0, 60
	s_nop 1
	v_writelane_b32 v235, s1, 61
	s_and_b64 s[0:1], s[0:1], s[2:3]
	s_andn2_b64 vcc, exec, s[0:1]
	v_writelane_b32 v235, s92, 62
	s_cbranch_vccnz .LBB0_496
	s_cmpk_gt_i32 s50, 0xa0
	s_cselect_b32 s0, 0x420, 0
	s_add_i32 s33, s0, s92
	s_cmpk_gt_i32 s33, 0x5ff
	s_mov_b32 s23, 0
	s_cbranch_scc1 .LBB0_336
	s_mov_b32 s6, s33
	s_mov_b32 s7, s50
	s_movk_i32 s8, 0x600
	v_readlane_b32 s9, v235, 52
	v_readlane_b32 s2, v235, 9
	v_readlane_b32 s3, v235, 10
	v_readlane_b32 s4, v235, 19
	v_readlane_b32 s5, v235, 20
	s_mov_b32 s72, 0x3e38aa3b
	s_mov_b32 s73, 0x3e38aa3b
	v_lshrrev_b32_e32 v2, 3, v0
	v_and_b32_e32 v3, 7, v0
	v_lshlrev_b32_e32 v3, 4, v3
	s_movk_i32 s39, 0x90
	v_mad_u32_u24 v1, v2, s39, v3
	v_and_b32_e32 v5, 0xff, v0
	v_lshrrev_b32_e32 v6, 8, v0
	s_movk_i32 s39, 0x1180
	v_mul_u32_u24_e32 v4, s39, v6
	v_lshl_add_u32 v4, v5, 1, v4
	v_add_u32_e32 v4, 0xe100, v4
	v_lshlrev_b32_e32 v6, 4, v6
	v_lshlrev_b32_e32 v8, 2, v5
	v_add_u32_e32 v8, 0x16d00, v8
	v_subrev_u32_e32 v165, 16, v0
	s_movk_i32 s39, 0x81
	v_cmp_gt_u32_e64 s[42:43], s39, v165
	s_movk_i32 s39, 0xa0
	v_cmp_gt_u32_e64 s[48:49], s39, v0
	v_cmp_gt_u32_e64 s[46:47], 64, v0
	v_cmp_gt_u32_e64 s[44:45], 16, v146
	v_subrev_u32_e32 v165, 0x50, v0
	v_cmp_lt_i32_e32 vcc, 0, v165
	v_mov_b32_e32 v7, 0
	s_nop 0
	v_cndmask_b32_e64 v166, 0, 16, vcc
	v_lshlrev_b32_e32 v167, 0, v165
	v_sub_u32_e32 v168, 0, v167
	v_max_i32_e32 v167, v167, v168
	v_cvt_f32_u32_e32 v168, v167
	v_mul_f32_e32 v168, 0x3e000000, v168
	v_max_f32_e32 v168, 1.0, v168
	v_log_f32_e32 v168, v168
	v_cmp_gt_u32_e32 vcc, 8, v167
	v_mul_f32_e32 v168, 0x3f924925, v168
	v_cvt_i32_f32_e32 v168, v168
	v_min_i32_e32 v168, 7, v168
	v_add_u32_e32 v168, 8, v168
	v_cndmask_b32_e32 v168, v168, v167, vcc
	v_add_u32_e32 v168, v168, v166
	v_lshl_or_b32 v7, v168, 0, v7
	v_lshlrev_b32_e32 v167, 2, v165
	v_sub_u32_e32 v168, 0, v167
	v_max_i32_e32 v167, v167, v168
	v_cvt_f32_u32_e32 v168, v167
	v_mul_f32_e32 v168, 0x3e000000, v168
	v_max_f32_e32 v168, 1.0, v168
	v_log_f32_e32 v168, v168
	v_cmp_gt_u32_e32 vcc, 8, v167
	v_mul_f32_e32 v168, 0x3f924925, v168
	v_cvt_i32_f32_e32 v168, v168
	v_min_i32_e32 v168, 7, v168
	v_add_u32_e32 v168, 8, v168
	v_cndmask_b32_e32 v168, v168, v167, vcc
	v_add_u32_e32 v168, v168, v166
	v_lshl_or_b32 v7, v168, 8, v7
	v_lshlrev_b32_e32 v167, 4, v165
	v_sub_u32_e32 v168, 0, v167
	v_max_i32_e32 v167, v167, v168
	v_cvt_f32_u32_e32 v168, v167
	v_mul_f32_e32 v168, 0x3e000000, v168
	v_max_f32_e32 v168, 1.0, v168
	v_log_f32_e32 v168, v168
	v_cmp_gt_u32_e32 vcc, 8, v167
	v_mul_f32_e32 v168, 0x3f924925, v168
	v_cvt_i32_f32_e32 v168, v168
	v_min_i32_e32 v168, 7, v168
	v_add_u32_e32 v168, 8, v168
	v_cndmask_b32_e32 v168, v168, v167, vcc
	v_add_u32_e32 v168, v168, v166
	v_lshl_or_b32 v7, v168, 16, v7
	v_and_b32_e32 v165, 15, v146
	v_lshrrev_b32_e32 v166, 4, v146
	s_lshl_b32 s39, s9, 4
	v_add_u32_e32 v40, s39, v165
	s_movk_i32 s40, 0x90
	v_mul_u32_u24_e32 v34, s40, v40
	v_lshl_add_u32 v34, v166, 4, v34
	v_lshlrev_b32_e32 v167, 2, v166
	v_sub_u32_e32 v35, v167, v165
	v_lshlrev_b32_e32 v35, 2, v35
	v_add_u32_e32 v35, 0x16d40, v35
	v_add_u32_e32 v167, s39, v167
	v_lshlrev_b32_e32 v36, 2, v167
	v_add_u32_e32 v36, 0x16f80, v36
	s_movk_i32 s40, 0x230
	v_mul_u32_u24_e32 v37, s40, v165
	v_lshl_add_u32 v37, v167, 1, v37
	v_add_u32_e32 v37, 0xe100, v37
	v_add_u32_e32 v9, 0x2300, v37
	v_add_u32_e32 v118, 0x4600, v37
	v_add_u32_e32 v144, 0x6900, v37
	v_xor_b32_e32 v38, 16, v146
	v_lshlrev_b32_e32 v38, 2, v38
	v_xor_b32_e32 v39, 32, v146
	v_lshlrev_b32_e32 v39, 2, v39
	v_lshlrev_b32_e32 v41, 3, v166
	v_mov_b32_e32 v232, 0
	v_mov_b32_e32 v233, 0
	s_movk_i32 s40, 0x230
	v_mul_u32_u24_e32 v168, s40, v0
	v_add_u32_e32 v168, 0xe300, v168
	s_and_saveexec_b64 s[40:41], s[46:47]
	ds_write_b64 v168, v[232:233] offset:0
	ds_write_b64 v168, v[232:233] offset:8
	ds_write_b64 v168, v[232:233] offset:16
	ds_write_b64 v168, v[232:233] offset:24
	s_mov_b64 exec, s[40:41]
	s_and_b32 s39, s6, 15
	s_bfe_u32 s40, s6, 0x20004
	s_bfe_u32 s41, s6, 0x30006
	s_lshr_b32 s74, s6, 9
	s_lshl_b32 s75, s74, 1
	s_add_i32 s16, s75, 13
	s_add_i32 s20, s75, 9
	s_add_i32 s26, s75, 4
	s_lshl_b32 s28, s74, 3
	s_lshr_b32 s29, 0x800, s75
	s_add_i32 s17, s29, -1
	s_sub_i32 s76, 4, s75
	s_lshr_b32 s77, s39, s76
	s_lshr_b32 s78, 16, s75
	s_add_i32 s78, s78, -1
	s_and_b32 s78, s39, s78
	s_lshl_b32 s19, s78, 7
	s_add_i32 s18, s19, 0xffffffc0
	s_lshl_b32 s79, s41, 11
	s_add_i32 s79, s79, s77
	s_lshl_b32 s80, s40, 7
	s_lshl_b32 s27, s40, 2
	s_lshl_b32 s81, s79, 13
	s_add_u32 s81, s81, s80
	s_add_u32 s81, s81, 0x2ca00000
	s_add_u32 s10, s2, s81
	s_addc_u32 s11, s3, 0
	s_lshl_b32 s82, s74, 14
	s_add_i32 s82, s82, s79
	s_lshl_b32 s83, s82, 9
	s_add_u32 s83, s83, s80
	s_add_u32 s83, s83, 0x34a00000
	s_add_u32 s12, s2, s83
	s_addc_u32 s13, s3, 0
	s_lshl_b32 s84, s82, 4
	s_add_u32 s84, s84, s27
	s_add_u32 s84, s84, 0x36200000
	s_add_u32 s14, s2, s84
	s_addc_u32 s15, s3, 0
	v_add_u32_e32 v165, s19, v2
	v_lshl_add_u32 v165, v165, s16, v3
	s_lshl_b32 s85, 64, s16
	global_load_dwordx4 v[120:123], v165, s[10:11]
	v_add_u32_e32 v166, s85, v165
	global_load_dwordx4 v[124:127], v166, s[10:11]
	v_add_u32_e32 v167, s18, v2
	v_med3_i32 v168, v167, 0, s17
	v_lshl_add_u32 v168, v168, s16, v3
	global_load_dwordx4 v[128:131], v168, s[10:11] offset:512
	v_add_u32_e32 v168, 64, v167
	v_med3_i32 v168, v168, 0, s17
	v_lshl_add_u32 v168, v168, s16, v3
	global_load_dwordx4 v[132:135], v168, s[10:11] offset:512
	v_add_u32_e32 v168, 0x80, v167
	v_med3_i32 v168, v168, 0, s17
	v_lshl_add_u32 v168, v168, s16, v3
	global_load_dwordx4 v[136:139], v168, s[10:11] offset:512
	v_add_u32_e32 v168, 0xc0, v167
	v_med3_i32 v168, v168, 0, s17
	v_lshl_add_u32 v168, v168, s16, v3
	global_load_dwordx4 v[140:143], v168, s[10:11] offset:512
	v_add_u32_e32 v169, s18, v5
	v_med3_i32 v169, v169, 0, s17
	v_lshl_add_u32 v169, v169, s16, v6
	global_load_dwordx4 v[148:151], v169, s[10:11] offset:1024
	global_load_dwordx4 v[152:155], v169, s[10:11] offset:1056
	global_load_dwordx4 v[156:159], v169, s[10:11] offset:1088
	global_load_dwordx4 v[160:163], v169, s[10:11] offset:1120
	v_bfe_u32 v171, v7, s28, 8
	v_lshl_add_u32 v171, v171, 4, s27
	s_mov_b64 exec, s[42:43]
	global_load_dword v164, v171, s[4:5]
	s_mov_b64 exec, -1

; #define LAS __attribute__((address_space(3)))
; DI void attn_unit(const Args& A, LAS unsigned char* lds, int unit, int tid, int wave, int lane) {
;     const bf16* Z = (const bf16*)(A.ws + WS_Z); bf16* ao = (bf16*)(A.ws + WS_ATTO); float* al = (float*)(A.ws + WS_ATTL);
;     const int x = unit & 15; int r0 = unit >> 4; const int hh = r0 & 3; r0 >>= 2; const int b = r0 % NB, br = r0 / NB;
;     const int dil = br == 0 ? 1 : (br == 1 ? 4 : 16), lsub = SEQ / dil, nblk = lsub / 128;
;     const int res = x / nblk, nbk = x % nblk, l0 = nbk * 128, wbase = l0 - 64;
;     LAS bf16* Qs = (LAS bf16*)(lds + AT_QS); LAS bf16* Ks = (LAS bf16*)(lds + AT_KS); LAS bf16* Vt = (LAS bf16*)(lds + AT_VT); LAS float* btab = (LAS float*)(lds + AT_BT);
;     __syncthreads();
; #pragma unroll
;     for (int i = 0; i < 2; ++i) { const int id = tid + 512 * i, row = id >> 3, ch = id & 7; const int tok = b * SEQ + (l0 + row) * dil + res;
;         *(LAS u32x4_t*)(Qs + row * AT_QLD + ch * 8) = *(const u32x4_t*)(Z + (size_t)tok * ZLD + ZA + hh * 64 + ch * 8); }
;     for (int id = tid; id < 272 * 8; id += NTHR) { const int row = id >> 3, ch = id & 7; const int pos = wbase + row; u32x4_t v = (u32x4_t){0u, 0u, 0u, 0u};
;         if (row < 256 && pos >= 0 && pos < lsub) v = *(const u32x4_t*)(Z + (size_t)(b * SEQ + pos * dil + res) * ZLD + ZA + 256 + hh * 64 + ch * 8);
;         *(LAS u32x4_t*)(Ks + row * AT_QLD + ch * 8) = v; }
;     for (int id = tid; id < 272 * 8; id += NTHR) { const int key = id % 272, ch = id / 272; const int pos = wbase + key; u32x4_t v = (u32x4_t){0u, 0u, 0u, 0u};
;         if (key < 256 && pos >= 0 && pos < lsub) v = *(const u32x4_t*)(Z + (size_t)(b * SEQ + pos * dil + res) * ZLD + ZA + 512 + hh * 64 + ch * 8);
;         LAS bf16* d = Vt + (ch * 8) * AT_VLD + key;
;         d[0] = (bf16)(v.x & 0xffffu); d[AT_VLD] = (bf16)(v.x >> 16); d[2 * AT_VLD] = (bf16)(v.y & 0xffffu); d[3 * AT_VLD] = (bf16)(v.y >> 16);
;         d[4 * AT_VLD] = (bf16)(v.z & 0xffffu); d[5 * AT_VLD] = (bf16)(v.z >> 16); d[6 * AT_VLD] = (bf16)(v.w & 0xffffu); d[7 * AT_VLD] = (bf16)(v.w >> 16); }
;     if (tid < 129) btab[tid] = A.in[I_RELB][t5_bucket((tid - 64) * dil) * 4 + hh] * 1.4426950408889634f;
;     __syncthreads();
.LBB0_546:
	s_cmp_lt_i32 s6, 5
	s_cselect_b64 s[94:95], -1, 0
	s_and_b64 s[0:1], s[94:95], s[0:1]
	s_andn2_b64 vcc, exec, s[0:1]
	s_cbranch_vccnz .LBB0_957
	s_cmpk_lt_i32 s50, 0xa1
	s_cselect_b64 s[0:1], -1, 0
	s_cmpk_lt_i32 s92, 0xa0
	s_cselect_b64 s[2:3], -1, 0
	s_or_b64 s[0:1], s[2:3], s[0:1]
	s_and_b64 vcc, exec, s[0:1]
	s_cbranch_vccnz .LBB0_640
	s_add_i32 s22, s92, 0xffffff60
	s_cmpk_gt_u32 s22, 0x23f
	s_cbranch_scc1 .LBB0_639
	s_mov_b32 s6, s22
	s_add_i32 s7, s50, 0xffffff60
	s_movk_i32 s8, 0x420
	v_readlane_b32 s9, v235, 52
	v_readlane_b32 s2, v235, 9
	v_readlane_b32 s3, v235, 10
	v_readlane_b32 s4, v235, 19
	v_readlane_b32 s5, v235, 20
	s_mov_b32 s72, 0x3e38aa3b
	s_mov_b32 s73, 0x3e38aa3b
	v_lshrrev_b32_e32 v2, 3, v0
	v_and_b32_e32 v3, 7, v0
	v_lshlrev_b32_e32 v3, 4, v3
	s_movk_i32 s39, 0x90
	v_mad_u32_u24 v1, v2, s39, v3
	v_and_b32_e32 v5, 0xff, v0
	v_lshrrev_b32_e32 v6, 8, v0
	s_movk_i32 s39, 0x1180
	v_mul_u32_u24_e32 v4, s39, v6
	v_lshl_add_u32 v4, v5, 1, v4
	v_add_u32_e32 v4, 0xe100, v4
	v_lshlrev_b32_e32 v6, 4, v6
	v_lshlrev_b32_e32 v8, 2, v5
	v_add_u32_e32 v8, 0x16d00, v8
	v_subrev_u32_e32 v165, 16, v0
	s_movk_i32 s39, 0x81
	v_cmp_gt_u32_e64 s[42:43], s39, v165
	s_movk_i32 s39, 0xa0
	v_cmp_gt_u32_e64 s[48:49], s39, v0
	v_cmp_gt_u32_e64 s[46:47], 64, v0
	v_cmp_gt_u32_e64 s[44:45], 16, v146
	v_subrev_u32_e32 v165, 0x50, v0
	v_cmp_lt_i32_e32 vcc, 0, v165
	v_mov_b32_e32 v7, 0
	s_nop 0
	v_cndmask_b32_e64 v166, 0, 16, vcc
	v_lshlrev_b32_e32 v167, 0, v165
	v_sub_u32_e32 v168, 0, v167
	v_max_i32_e32 v167, v167, v168
	v_cvt_f32_u32_e32 v168, v167
	v_mul_f32_e32 v168, 0x3e000000, v168
	v_max_f32_e32 v168, 1.0, v168
	v_log_f32_e32 v168, v168
	v_cmp_gt_u32_e32 vcc, 8, v167
	v_mul_f32_e32 v168, 0x3f924925, v168
	v_cvt_i32_f32_e32 v168, v168
	v_min_i32_e32 v168, 7, v168
	v_add_u32_e32 v168, 8, v168
	v_cndmask_b32_e32 v168, v168, v167, vcc
	v_add_u32_e32 v168, v168, v166
	v_lshl_or_b32 v7, v168, 0, v7
	v_lshlrev_b32_e32 v167, 2, v165
	v_sub_u32_e32 v168, 0, v167
	v_max_i32_e32 v167, v167, v168
	v_cvt_f32_u32_e32 v168, v167
	v_mul_f32_e32 v168, 0x3e000000, v168
	v_max_f32_e32 v168, 1.0, v168
	v_log_f32_e32 v168, v168
	v_cmp_gt_u32_e32 vcc, 8, v167
	v_mul_f32_e32 v168, 0x3f924925, v168
	v_cvt_i32_f32_e32 v168, v168
	v_min_i32_e32 v168, 7, v168
	v_add_u32_e32 v168, 8, v168
	v_cndmask_b32_e32 v168, v168, v167, vcc
	v_add_u32_e32 v168, v168, v166
	v_lshl_or_b32 v7, v168, 8, v7
	v_lshlrev_b32_e32 v167, 4, v165
	v_sub_u32_e32 v168, 0, v167
	v_max_i32_e32 v167, v167, v168
	v_cvt_f32_u32_e32 v168, v167
	v_mul_f32_e32 v168, 0x3e000000, v168
	v_max_f32_e32 v168, 1.0, v168
	v_log_f32_e32 v168, v168
	v_cmp_gt_u32_e32 vcc, 8, v167
	v_mul_f32_e32 v168, 0x3f924925, v168
	v_cvt_i32_f32_e32 v168, v168
	v_min_i32_e32 v168, 7, v168
	v_add_u32_e32 v168, 8, v168
	v_cndmask_b32_e32 v168, v168, v167, vcc
	v_add_u32_e32 v168, v168, v166
	v_lshl_or_b32 v7, v168, 16, v7
	v_and_b32_e32 v165, 15, v146
	v_lshrrev_b32_e32 v166, 4, v146
	s_lshl_b32 s39, s9, 4
	v_add_u32_e32 v40, s39, v165
	s_movk_i32 s40, 0x90
	v_mul_u32_u24_e32 v34, s40, v40
	v_lshl_add_u32 v34, v166, 4, v34
	v_lshlrev_b32_e32 v167, 2, v166
	v_sub_u32_e32 v35, v167, v165
	v_lshlrev_b32_e32 v35, 2, v35
	v_add_u32_e32 v35, 0x16d40, v35
	v_add_u32_e32 v167, s39, v167
	v_lshlrev_b32_e32 v36, 2, v167
	v_add_u32_e32 v36, 0x16f80, v36
	s_movk_i32 s40, 0x230
	v_mul_u32_u24_e32 v37, s40, v165
	v_lshl_add_u32 v37, v167, 1, v37
	v_add_u32_e32 v37, 0xe100, v37
	v_add_u32_e32 v9, 0x2300, v37
	v_add_u32_e32 v118, 0x4600, v37
	v_add_u32_e32 v144, 0x6900, v37
	v_xor_b32_e32 v38, 16, v146
	v_lshlrev_b32_e32 v38, 2, v38
	v_xor_b32_e32 v39, 32, v146
	v_lshlrev_b32_e32 v39, 2, v39
	v_lshlrev_b32_e32 v41, 3, v166
	v_mov_b32_e32 v232, 0
	v_mov_b32_e32 v233, 0
	s_movk_i32 s40, 0x230
	v_mul_u32_u24_e32 v168, s40, v0
	v_add_u32_e32 v168, 0xe300, v168
	s_and_saveexec_b64 s[40:41], s[46:47]
	ds_write_b64 v168, v[232:233] offset:0
	ds_write_b64 v168, v[232:233] offset:8
	ds_write_b64 v168, v[232:233] offset:16
	ds_write_b64 v168, v[232:233] offset:24
	s_mov_b64 exec, s[40:41]
	s_and_b32 s39, s6, 15
	s_bfe_u32 s40, s6, 0x20004
	s_bfe_u32 s41, s6, 0x30006
	s_lshr_b32 s74, s6, 9
	s_lshl_b32 s75, s74, 1
	s_add_i32 s16, s75, 13
	s_add_i32 s20, s75, 9
	s_add_i32 s26, s75, 4
	s_lshl_b32 s28, s74, 3
	s_lshr_b32 s29, 0x800, s75
	s_add_i32 s17, s29, -1
	s_sub_i32 s76, 4, s75
	s_lshr_b32 s77, s39, s76
	s_lshr_b32 s78, 16, s75
	s_add_i32 s78, s78, -1
	s_and_b32 s78, s39, s78
	s_lshl_b32 s19, s78, 7
	s_add_i32 s18, s19, 0xffffffc0
	s_lshl_b32 s79, s41, 11
	s_add_i32 s79, s79, s77
	s_lshl_b32 s80, s40, 7
	s_lshl_b32 s27, s40, 2
	s_lshl_b32 s81, s79, 13
	s_add_u32 s81, s81, s80
	s_add_u32 s81, s81, 0x2ca00000
	s_add_u32 s10, s2, s81
	s_addc_u32 s11, s3, 0
	s_lshl_b32 s82, s74, 14
	s_add_i32 s82, s82, s79
	s_lshl_b32 s83, s82, 9
	s_add_u32 s83, s83, s80
	s_add_u32 s83, s83, 0x34a00000
	s_add_u32 s12, s2, s83
	s_addc_u32 s13, s3, 0
	s_lshl_b32 s84, s82, 4
	s_add_u32 s84, s84, s27
	s_add_u32 s84, s84, 0x36200000
	s_add_u32 s14, s2, s84
	s_addc_u32 s15, s3, 0
	v_add_u32_e32 v165, s19, v2
	v_lshl_add_u32 v165, v165, s16, v3
	s_lshl_b32 s85, 64, s16
	global_load_dwordx4 v[120:123], v165, s[10:11]
	v_add_u32_e32 v166, s85, v165
	global_load_dwordx4 v[124:127], v166, s[10:11]
	v_add_u32_e32 v167, s18, v2
	v_med3_i32 v168, v167, 0, s17
	v_lshl_add_u32 v168, v168, s16, v3
	global_load_dwordx4 v[128:131], v168, s[10:11] offset:512
	v_add_u32_e32 v168, 64, v167
	v_med3_i32 v168, v168, 0, s17
	v_lshl_add_u32 v168, v168, s16, v3
	global_load_dwordx4 v[132:135], v168, s[10:11] offset:512
	v_add_u32_e32 v168, 0x80, v167
	v_med3_i32 v168, v168, 0, s17
	v_lshl_add_u32 v168, v168, s16, v3
	global_load_dwordx4 v[136:139], v168, s[10:11] offset:512
	v_add_u32_e32 v168, 0xc0, v167
	v_med3_i32 v168, v168, 0, s17
	v_lshl_add_u32 v168, v168, s16, v3
	global_load_dwordx4 v[140:143], v168, s[10:11] offset:512
	v_add_u32_e32 v169, s18, v5
	v_med3_i32 v169, v169, 0, s17
	v_lshl_add_u32 v169, v169, s16, v6
	global_load_dwordx4 v[148:151], v169, s[10:11] offset:1024
	global_load_dwordx4 v[152:155], v169, s[10:11] offset:1056
	global_load_dwordx4 v[156:159], v169, s[10:11] offset:1088
	global_load_dwordx4 v[160:163], v169, s[10:11] offset:1120
	v_bfe_u32 v171, v7, s28, 8
	v_lshl_add_u32 v171, v171, 4, s27
	s_mov_b64 exec, s[42:43]
	global_load_dword v164, v171, s[4:5]
	s_mov_b64 exec, -1

; #define LAS __attribute__((address_space(3)))
; DI void attn_unit(const Args& A, LAS unsigned char* lds, int unit, int tid, int wave, int lane) {
;     const bf16* Z = (const bf16*)(A.ws + WS_Z); bf16* ao = (bf16*)(A.ws + WS_ATTO); float* al = (float*)(A.ws + WS_ATTL);
;     const int x = unit & 15; int r0 = unit >> 4; const int hh = r0 & 3; r0 >>= 2; const int b = r0 % NB, br = r0 / NB;
;     const int dil = br == 0 ? 1 : (br == 1 ? 4 : 16), lsub = SEQ / dil, nblk = lsub / 128;
;     const int res = x / nblk, nbk = x % nblk, l0 = nbk * 128, wbase = l0 - 64;
;     LAS bf16* Qs = (LAS bf16*)(lds + AT_QS); LAS bf16* Ks = (LAS bf16*)(lds + AT_KS); LAS bf16* Vt = (LAS bf16*)(lds + AT_VT); LAS float* btab = (LAS float*)(lds + AT_BT);
;     __syncthreads();
; #pragma unroll
;     for (int i = 0; i < 2; ++i) { const int id = tid + 512 * i, row = id >> 3, ch = id & 7; const int tok = b * SEQ + (l0 + row) * dil + res;
;         *(LAS u32x4_t*)(Qs + row * AT_QLD + ch * 8) = *(const u32x4_t*)(Z + (size_t)tok * ZLD + ZA + hh * 64 + ch * 8); }
;     for (int id = tid; id < 272 * 8; id += NTHR) { const int row = id >> 3, ch = id & 7; const int pos = wbase + row; u32x4_t v = (u32x4_t){0u, 0u, 0u, 0u};
;         if (row < 256 && pos >= 0 && pos < lsub) v = *(const u32x4_t*)(Z + (size_t)(b * SEQ + pos * dil + res) * ZLD + ZA + 256 + hh * 64 + ch * 8);
;         *(LAS u32x4_t*)(Ks + row * AT_QLD + ch * 8) = v; }
;     for (int id = tid; id < 272 * 8; id += NTHR) { const int key = id % 272, ch = id / 272; const int pos = wbase + key; u32x4_t v = (u32x4_t){0u, 0u, 0u, 0u};
;         if (key < 256 && pos >= 0 && pos < lsub) v = *(const u32x4_t*)(Z + (size_t)(b * SEQ + pos * dil + res) * ZLD + ZA + 512 + hh * 64 + ch * 8);
;         LAS bf16* d = Vt + (ch * 8) * AT_VLD + key;
;         d[0] = (bf16)(v.x & 0xffffu); d[AT_VLD] = (bf16)(v.x >> 16); d[2 * AT_VLD] = (bf16)(v.y & 0xffffu); d[3 * AT_VLD] = (bf16)(v.y >> 16);
;         d[4 * AT_VLD] = (bf16)(v.z & 0xffffu); d[5 * AT_VLD] = (bf16)(v.z >> 16); d[6 * AT_VLD] = (bf16)(v.w & 0xffffu); d[7 * AT_VLD] = (bf16)(v.w >> 16); }
;     if (tid < 129) btab[tid] = A.in[I_RELB][t5_bucket((tid - 64) * dil) * 4 + hh] * 1.4426950408889634f;
;     __syncthreads();
.LBB0_1704:
	s_cmp_lt_i32 s6, 14
	s_cselect_b64 s[0:1], -1, 0
	v_writelane_b32 v234, s0, 44
	s_nop 1
	v_writelane_b32 v234, s1, 45
	s_and_b64 s[0:1], s[0:1], s[2:3]
	s_andn2_b64 vcc, exec, s[0:1]
	s_cbranch_vccnz .LBB0_1958
	s_cmpk_gt_i32 s50, 0xa0
	s_cselect_b32 s0, 0x420, 0
	s_add_i32 s33, s0, s92
	s_cmpk_gt_i32 s33, 0x5ff
	s_mov_b32 s3, 0
	s_cbranch_scc1 .LBB0_1796
	s_mov_b32 s6, s33
	s_mov_b32 s7, s50
	s_movk_i32 s8, 0x600
	v_readlane_b32 s9, v235, 52
	v_readlane_b32 s2, v235, 9
	v_readlane_b32 s3, v235, 10
	v_readlane_b32 s4, v235, 19
	v_readlane_b32 s5, v235, 20
	s_mov_b32 s72, 0x3e38aa3b
	s_mov_b32 s73, 0x3e38aa3b
	v_lshrrev_b32_e32 v2, 3, v0
	v_and_b32_e32 v3, 7, v0
	v_lshlrev_b32_e32 v3, 4, v3
	s_movk_i32 s39, 0x90
	v_mad_u32_u24 v1, v2, s39, v3
	v_and_b32_e32 v5, 0xff, v0
	v_lshrrev_b32_e32 v6, 8, v0
	s_movk_i32 s39, 0x1180
	v_mul_u32_u24_e32 v4, s39, v6
	v_lshl_add_u32 v4, v5, 1, v4
	v_add_u32_e32 v4, 0xe100, v4
	v_lshlrev_b32_e32 v6, 4, v6
	v_lshlrev_b32_e32 v8, 2, v5
	v_add_u32_e32 v8, 0x16d00, v8
	v_subrev_u32_e32 v165, 16, v0
	s_movk_i32 s39, 0x81
	v_cmp_gt_u32_e64 s[42:43], s39, v165
	s_movk_i32 s39, 0xa0
	v_cmp_gt_u32_e64 s[48:49], s39, v0
	v_cmp_gt_u32_e64 s[46:47], 64, v0
	v_cmp_gt_u32_e64 s[44:45], 16, v146
	v_subrev_u32_e32 v165, 0x50, v0
	v_cmp_lt_i32_e32 vcc, 0, v165
	v_mov_b32_e32 v7, 0
	s_nop 0
	v_cndmask_b32_e64 v166, 0, 16, vcc
	v_lshlrev_b32_e32 v167, 0, v165
	v_sub_u32_e32 v168, 0, v167
	v_max_i32_e32 v167, v167, v168
	v_cvt_f32_u32_e32 v168, v167
	v_mul_f32_e32 v168, 0x3e000000, v168
	v_max_f32_e32 v168, 1.0, v168
	v_log_f32_e32 v168, v168
	v_cmp_gt_u32_e32 vcc, 8, v167
	v_mul_f32_e32 v168, 0x3f924925, v168
	v_cvt_i32_f32_e32 v168, v168
	v_min_i32_e32 v168, 7, v168
	v_add_u32_e32 v168, 8, v168
	v_cndmask_b32_e32 v168, v168, v167, vcc
	v_add_u32_e32 v168, v168, v166
	v_lshl_or_b32 v7, v168, 0, v7
	v_lshlrev_b32_e32 v167, 2, v165
	v_sub_u32_e32 v168, 0, v167
	v_max_i32_e32 v167, v167, v168
	v_cvt_f32_u32_e32 v168, v167
	v_mul_f32_e32 v168, 0x3e000000, v168
	v_max_f32_e32 v168, 1.0, v168
	v_log_f32_e32 v168, v168
	v_cmp_gt_u32_e32 vcc, 8, v167
	v_mul_f32_e32 v168, 0x3f924925, v168
	v_cvt_i32_f32_e32 v168, v168
	v_min_i32_e32 v168, 7, v168
	v_add_u32_e32 v168, 8, v168
	v_cndmask_b32_e32 v168, v168, v167, vcc
	v_add_u32_e32 v168, v168, v166
	v_lshl_or_b32 v7, v168, 8, v7
	v_lshlrev_b32_e32 v167, 4, v165
	v_sub_u32_e32 v168, 0, v167
	v_max_i32_e32 v167, v167, v168
	v_cvt_f32_u32_e32 v168, v167
	v_mul_f32_e32 v168, 0x3e000000, v168
	v_max_f32_e32 v168, 1.0, v168
	v_log_f32_e32 v168, v168
	v_cmp_gt_u32_e32 vcc, 8, v167
	v_mul_f32_e32 v168, 0x3f924925, v168
	v_cvt_i32_f32_e32 v168, v168
	v_min_i32_e32 v168, 7, v168
	v_add_u32_e32 v168, 8, v168
	v_cndmask_b32_e32 v168, v168, v167, vcc
	v_add_u32_e32 v168, v168, v166
	v_lshl_or_b32 v7, v168, 16, v7
	v_and_b32_e32 v165, 15, v146
	v_lshrrev_b32_e32 v166, 4, v146
	s_lshl_b32 s39, s9, 4
	v_add_u32_e32 v40, s39, v165
	s_movk_i32 s40, 0x90
	v_mul_u32_u24_e32 v34, s40, v40
	v_lshl_add_u32 v34, v166, 4, v34
	v_lshlrev_b32_e32 v167, 2, v166
	v_sub_u32_e32 v35, v167, v165
	v_lshlrev_b32_e32 v35, 2, v35
	v_add_u32_e32 v35, 0x16d40, v35
	v_add_u32_e32 v167, s39, v167
	v_lshlrev_b32_e32 v36, 2, v167
	v_add_u32_e32 v36, 0x16f80, v36
	s_movk_i32 s40, 0x230
	v_mul_u32_u24_e32 v37, s40, v165
	v_lshl_add_u32 v37, v167, 1, v37
	v_add_u32_e32 v37, 0xe100, v37
	v_add_u32_e32 v9, 0x2300, v37
	v_add_u32_e32 v118, 0x4600, v37
	v_add_u32_e32 v144, 0x6900, v37
	v_xor_b32_e32 v38, 16, v146
	v_lshlrev_b32_e32 v38, 2, v38
	v_xor_b32_e32 v39, 32, v146
	v_lshlrev_b32_e32 v39, 2, v39
	v_lshlrev_b32_e32 v41, 3, v166
	v_mov_b32_e32 v232, 0
	v_mov_b32_e32 v233, 0
	s_movk_i32 s40, 0x230
	v_mul_u32_u24_e32 v168, s40, v0
	v_add_u32_e32 v168, 0xe300, v168
	s_and_saveexec_b64 s[40:41], s[46:47]
	ds_write_b64 v168, v[232:233] offset:0
	ds_write_b64 v168, v[232:233] offset:8
	ds_write_b64 v168, v[232:233] offset:16
	ds_write_b64 v168, v[232:233] offset:24
	s_mov_b64 exec, s[40:41]
	s_and_b32 s39, s6, 15
	s_bfe_u32 s40, s6, 0x20004
	s_bfe_u32 s41, s6, 0x30006
	s_lshr_b32 s74, s6, 9
	s_lshl_b32 s75, s74, 1
	s_add_i32 s16, s75, 13
	s_add_i32 s20, s75, 9
	s_add_i32 s26, s75, 4
	s_lshl_b32 s28, s74, 3
	s_lshr_b32 s29, 0x800, s75
	s_add_i32 s17, s29, -1
	s_sub_i32 s76, 4, s75
	s_lshr_b32 s77, s39, s76
	s_lshr_b32 s78, 16, s75
	s_add_i32 s78, s78, -1
	s_and_b32 s78, s39, s78
	s_lshl_b32 s19, s78, 7
	s_add_i32 s18, s19, 0xffffffc0
	s_lshl_b32 s79, s41, 11
	s_add_i32 s79, s79, s77
	s_lshl_b32 s80, s40, 7
	s_lshl_b32 s27, s40, 2
	s_lshl_b32 s81, s79, 13
	s_add_u32 s81, s81, s80
	s_add_u32 s81, s81, 0x2ca00000
	s_add_u32 s10, s2, s81
	s_addc_u32 s11, s3, 0
	s_lshl_b32 s82, s74, 14
	s_add_i32 s82, s82, s79
	s_lshl_b32 s83, s82, 9
	s_add_u32 s83, s83, s80
	s_add_u32 s83, s83, 0x34a00000
	s_add_u32 s12, s2, s83
	s_addc_u32 s13, s3, 0
	s_lshl_b32 s84, s82, 4
	s_add_u32 s84, s84, s27
	s_add_u32 s84, s84, 0x36200000
	s_add_u32 s14, s2, s84
	s_addc_u32 s15, s3, 0
	v_add_u32_e32 v165, s19, v2
	v_lshl_add_u32 v165, v165, s16, v3
	s_lshl_b32 s85, 64, s16
	global_load_dwordx4 v[120:123], v165, s[10:11]
	v_add_u32_e32 v166, s85, v165
	global_load_dwordx4 v[124:127], v166, s[10:11]
	v_add_u32_e32 v167, s18, v2
	v_med3_i32 v168, v167, 0, s17
	v_lshl_add_u32 v168, v168, s16, v3
	global_load_dwordx4 v[128:131], v168, s[10:11] offset:512
	v_add_u32_e32 v168, 64, v167
	v_med3_i32 v168, v168, 0, s17
	v_lshl_add_u32 v168, v168, s16, v3
	global_load_dwordx4 v[132:135], v168, s[10:11] offset:512
	v_add_u32_e32 v168, 0x80, v167
	v_med3_i32 v168, v168, 0, s17
	v_lshl_add_u32 v168, v168, s16, v3
	global_load_dwordx4 v[136:139], v168, s[10:11] offset:512
	v_add_u32_e32 v168, 0xc0, v167
	v_med3_i32 v168, v168, 0, s17
	v_lshl_add_u32 v168, v168, s16, v3
	global_load_dwordx4 v[140:143], v168, s[10:11] offset:512
	v_add_u32_e32 v169, s18, v5
	v_med3_i32 v169, v169, 0, s17
	v_lshl_add_u32 v169, v169, s16, v6
	global_load_dwordx4 v[148:151], v169, s[10:11] offset:1024
	global_load_dwordx4 v[152:155], v169, s[10:11] offset:1056
	global_load_dwordx4 v[156:159], v169, s[10:11] offset:1088
	global_load_dwordx4 v[160:163], v169, s[10:11] offset:1120
	v_bfe_u32 v171, v7, s28, 8
	v_lshl_add_u32 v171, v171, 4, s27
	s_mov_b64 exec, s[42:43]
	global_load_dword v164, v171, s[4:5]
	s_mov_b64 exec, -1

; #define LAS __attribute__((address_space(3)))
; DI void attn_unit(const Args& A, LAS unsigned char* lds, int unit, int tid, int wave, int lane) {
;     const bf16* Z = (const bf16*)(A.ws + WS_Z); bf16* ao = (bf16*)(A.ws + WS_ATTO); float* al = (float*)(A.ws + WS_ATTL);
;     const int x = unit & 15; int r0 = unit >> 4; const int hh = r0 & 3; r0 >>= 2; const int b = r0 % NB, br = r0 / NB;
;     const int dil = br == 0 ? 1 : (br == 1 ? 4 : 16), lsub = SEQ / dil, nblk = lsub / 128;
;     const int res = x / nblk, nbk = x % nblk, l0 = nbk * 128, wbase = l0 - 64;
;     LAS bf16* Qs = (LAS bf16*)(lds + AT_QS); LAS bf16* Ks = (LAS bf16*)(lds + AT_KS); LAS bf16* Vt = (LAS bf16*)(lds + AT_VT); LAS float* btab = (LAS float*)(lds + AT_BT);
;     __syncthreads();
; #pragma unroll
;     for (int i = 0; i < 2; ++i) { const int id = tid + 512 * i, row = id >> 3, ch = id & 7; const int tok = b * SEQ + (l0 + row) * dil + res;
;         *(LAS u32x4_t*)(Qs + row * AT_QLD + ch * 8) = *(const u32x4_t*)(Z + (size_t)tok * ZLD + ZA + hh * 64 + ch * 8); }
;     for (int id = tid; id < 272 * 8; id += NTHR) { const int row = id >> 3, ch = id & 7; const int pos = wbase + row; u32x4_t v = (u32x4_t){0u, 0u, 0u, 0u};
;         if (row < 256 && pos >= 0 && pos < lsub) v = *(const u32x4_t*)(Z + (size_t)(b * SEQ + pos * dil + res) * ZLD + ZA + 256 + hh * 64 + ch * 8);
;         *(LAS u32x4_t*)(Ks + row * AT_QLD + ch * 8) = v; }
;     for (int id = tid; id < 272 * 8; id += NTHR) { const int key = id % 272, ch = id / 272; const int pos = wbase + key; u32x4_t v = (u32x4_t){0u, 0u, 0u, 0u};
;         if (key < 256 && pos >= 0 && pos < lsub) v = *(const u32x4_t*)(Z + (size_t)(b * SEQ + pos * dil + res) * ZLD + ZA + 512 + hh * 64 + ch * 8);
;         LAS bf16* d = Vt + (ch * 8) * AT_VLD + key;
;         d[0] = (bf16)(v.x & 0xffffu); d[AT_VLD] = (bf16)(v.x >> 16); d[2 * AT_VLD] = (bf16)(v.y & 0xffffu); d[3 * AT_VLD] = (bf16)(v.y >> 16);
;         d[4 * AT_VLD] = (bf16)(v.z & 0xffffu); d[5 * AT_VLD] = (bf16)(v.z >> 16); d[6 * AT_VLD] = (bf16)(v.w & 0xffffu); d[7 * AT_VLD] = (bf16)(v.w >> 16); }
;     if (tid < 129) btab[tid] = A.in[I_RELB][t5_bucket((tid - 64) * dil) * 4 + hh] * 1.4426950408889634f;
;     __syncthreads();
.LBB0_2008:
	s_cmp_lt_i32 s6, 15
	s_cselect_b64 s[24:25], -1, 0
	s_and_b64 s[0:1], s[24:25], s[0:1]
	s_andn2_b64 vcc, exec, s[0:1]
	s_cbranch_vccnz .LBB0_2420
	s_cmpk_lt_i32 s50, 0xa1
	s_cselect_b64 s[0:1], -1, 0
	s_cmpk_lt_i32 s92, 0xa0
	s_cselect_b64 s[2:3], -1, 0
	s_or_b64 s[0:1], s[2:3], s[0:1]
	s_and_b64 vcc, exec, s[0:1]
	s_cbranch_vccnz .LBB0_2102
	s_add_i32 s33, s92, 0xffffff60
	s_cmpk_gt_u32 s33, 0x23f
	s_cbranch_scc1 .LBB0_2101
	s_mov_b32 s6, s33
	s_add_i32 s7, s50, 0xffffff60
	s_movk_i32 s8, 0x420
	v_readlane_b32 s9, v235, 52
	v_readlane_b32 s2, v235, 9
	v_readlane_b32 s3, v235, 10
	v_readlane_b32 s4, v235, 19
	v_readlane_b32 s5, v235, 20
	s_mov_b32 s72, 0x3e38aa3b
	s_mov_b32 s73, 0x3e38aa3b
	v_lshrrev_b32_e32 v2, 3, v0
	v_and_b32_e32 v3, 7, v0
	v_lshlrev_b32_e32 v3, 4, v3
	s_movk_i32 s39, 0x90
	v_mad_u32_u24 v1, v2, s39, v3
	v_and_b32_e32 v5, 0xff, v0
	v_lshrrev_b32_e32 v6, 8, v0
	s_movk_i32 s39, 0x1180
	v_mul_u32_u24_e32 v4, s39, v6
	v_lshl_add_u32 v4, v5, 1, v4
	v_add_u32_e32 v4, 0xe100, v4
	v_lshlrev_b32_e32 v6, 4, v6
	v_lshlrev_b32_e32 v8, 2, v5
	v_add_u32_e32 v8, 0x16d00, v8
	v_subrev_u32_e32 v165, 16, v0
	s_movk_i32 s39, 0x81
	v_cmp_gt_u32_e64 s[42:43], s39, v165
	s_movk_i32 s39, 0xa0
	v_cmp_gt_u32_e64 s[48:49], s39, v0
	v_cmp_gt_u32_e64 s[46:47], 64, v0
	v_cmp_gt_u32_e64 s[44:45], 16, v146
	v_subrev_u32_e32 v165, 0x50, v0
	v_cmp_lt_i32_e32 vcc, 0, v165
	v_mov_b32_e32 v7, 0
	s_nop 0
	v_cndmask_b32_e64 v166, 0, 16, vcc
	v_lshlrev_b32_e32 v167, 0, v165
	v_sub_u32_e32 v168, 0, v167
	v_max_i32_e32 v167, v167, v168
	v_cvt_f32_u32_e32 v168, v167
	v_mul_f32_e32 v168, 0x3e000000, v168
	v_max_f32_e32 v168, 1.0, v168
	v_log_f32_e32 v168, v168
	v_cmp_gt_u32_e32 vcc, 8, v167
	v_mul_f32_e32 v168, 0x3f924925, v168
	v_cvt_i32_f32_e32 v168, v168
	v_min_i32_e32 v168, 7, v168
	v_add_u32_e32 v168, 8, v168
	v_cndmask_b32_e32 v168, v168, v167, vcc
	v_add_u32_e32 v168, v168, v166
	v_lshl_or_b32 v7, v168, 0, v7
	v_lshlrev_b32_e32 v167, 2, v165
	v_sub_u32_e32 v168, 0, v167
	v_max_i32_e32 v167, v167, v168
	v_cvt_f32_u32_e32 v168, v167
	v_mul_f32_e32 v168, 0x3e000000, v168
	v_max_f32_e32 v168, 1.0, v168
	v_log_f32_e32 v168, v168
	v_cmp_gt_u32_e32 vcc, 8, v167
	v_mul_f32_e32 v168, 0x3f924925, v168
	v_cvt_i32_f32_e32 v168, v168
	v_min_i32_e32 v168, 7, v168
	v_add_u32_e32 v168, 8, v168
	v_cndmask_b32_e32 v168, v168, v167, vcc
	v_add_u32_e32 v168, v168, v166
	v_lshl_or_b32 v7, v168, 8, v7
	v_lshlrev_b32_e32 v167, 4, v165
	v_sub_u32_e32 v168, 0, v167
	v_max_i32_e32 v167, v167, v168
	v_cvt_f32_u32_e32 v168, v167
	v_mul_f32_e32 v168, 0x3e000000, v168
	v_max_f32_e32 v168, 1.0, v168
	v_log_f32_e32 v168, v168
	v_cmp_gt_u32_e32 vcc, 8, v167
	v_mul_f32_e32 v168, 0x3f924925, v168
	v_cvt_i32_f32_e32 v168, v168
	v_min_i32_e32 v168, 7, v168
	v_add_u32_e32 v168, 8, v168
	v_cndmask_b32_e32 v168, v168, v167, vcc
	v_add_u32_e32 v168, v168, v166
	v_lshl_or_b32 v7, v168, 16, v7
	v_and_b32_e32 v165, 15, v146
	v_lshrrev_b32_e32 v166, 4, v146
	s_lshl_b32 s39, s9, 4
	v_add_u32_e32 v40, s39, v165
	s_movk_i32 s40, 0x90
	v_mul_u32_u24_e32 v34, s40, v40
	v_lshl_add_u32 v34, v166, 4, v34
	v_lshlrev_b32_e32 v167, 2, v166
	v_sub_u32_e32 v35, v167, v165
	v_lshlrev_b32_e32 v35, 2, v35
	v_add_u32_e32 v35, 0x16d40, v35
	v_add_u32_e32 v167, s39, v167
	v_lshlrev_b32_e32 v36, 2, v167
	v_add_u32_e32 v36, 0x16f80, v36
	s_movk_i32 s40, 0x230
	v_mul_u32_u24_e32 v37, s40, v165
	v_lshl_add_u32 v37, v167, 1, v37
	v_add_u32_e32 v37, 0xe100, v37
	v_add_u32_e32 v9, 0x2300, v37
	v_add_u32_e32 v118, 0x4600, v37
	v_add_u32_e32 v144, 0x6900, v37
	v_xor_b32_e32 v38, 16, v146
	v_lshlrev_b32_e32 v38, 2, v38
	v_xor_b32_e32 v39, 32, v146
	v_lshlrev_b32_e32 v39, 2, v39
	v_lshlrev_b32_e32 v41, 3, v166
	v_mov_b32_e32 v232, 0
	v_mov_b32_e32 v233, 0
	s_movk_i32 s40, 0x230
	v_mul_u32_u24_e32 v168, s40, v0
	v_add_u32_e32 v168, 0xe300, v168
	s_and_saveexec_b64 s[40:41], s[46:47]
	ds_write_b64 v168, v[232:233] offset:0
	ds_write_b64 v168, v[232:233] offset:8
	ds_write_b64 v168, v[232:233] offset:16
	ds_write_b64 v168, v[232:233] offset:24
	s_mov_b64 exec, s[40:41]
	s_and_b32 s39, s6, 15
	s_bfe_u32 s40, s6, 0x20004
	s_bfe_u32 s41, s6, 0x30006
	s_lshr_b32 s74, s6, 9
	s_lshl_b32 s75, s74, 1
	s_add_i32 s16, s75, 13
	s_add_i32 s20, s75, 9
	s_add_i32 s26, s75, 4
	s_lshl_b32 s28, s74, 3
	s_lshr_b32 s29, 0x800, s75
	s_add_i32 s17, s29, -1
	s_sub_i32 s76, 4, s75
	s_lshr_b32 s77, s39, s76
	s_lshr_b32 s78, 16, s75
	s_add_i32 s78, s78, -1
	s_and_b32 s78, s39, s78
	s_lshl_b32 s19, s78, 7
	s_add_i32 s18, s19, 0xffffffc0
	s_lshl_b32 s79, s41, 11
	s_add_i32 s79, s79, s77
	s_lshl_b32 s80, s40, 7
	s_lshl_b32 s27, s40, 2
	s_lshl_b32 s81, s79, 13
	s_add_u32 s81, s81, s80
	s_add_u32 s81, s81, 0x2ca00000
	s_add_u32 s10, s2, s81
	s_addc_u32 s11, s3, 0
	s_lshl_b32 s82, s74, 14
	s_add_i32 s82, s82, s79
	s_lshl_b32 s83, s82, 9
	s_add_u32 s83, s83, s80
	s_add_u32 s83, s83, 0x34a00000
	s_add_u32 s12, s2, s83
	s_addc_u32 s13, s3, 0
	s_lshl_b32 s84, s82, 4
	s_add_u32 s84, s84, s27
	s_add_u32 s84, s84, 0x36200000
	s_add_u32 s14, s2, s84
	s_addc_u32 s15, s3, 0
	v_add_u32_e32 v165, s19, v2
	v_lshl_add_u32 v165, v165, s16, v3
	s_lshl_b32 s85, 64, s16
	global_load_dwordx4 v[120:123], v165, s[10:11]
	v_add_u32_e32 v166, s85, v165
	global_load_dwordx4 v[124:127], v166, s[10:11]
	v_add_u32_e32 v167, s18, v2
	v_med3_i32 v168, v167, 0, s17
	v_lshl_add_u32 v168, v168, s16, v3
	global_load_dwordx4 v[128:131], v168, s[10:11] offset:512
	v_add_u32_e32 v168, 64, v167
	v_med3_i32 v168, v168, 0, s17
	v_lshl_add_u32 v168, v168, s16, v3
	global_load_dwordx4 v[132:135], v168, s[10:11] offset:512
	v_add_u32_e32 v168, 0x80, v167
	v_med3_i32 v168, v168, 0, s17
	v_lshl_add_u32 v168, v168, s16, v3
	global_load_dwordx4 v[136:139], v168, s[10:11] offset:512
	v_add_u32_e32 v168, 0xc0, v167
	v_med3_i32 v168, v168, 0, s17
	v_lshl_add_u32 v168, v168, s16, v3
	global_load_dwordx4 v[140:143], v168, s[10:11] offset:512
	v_add_u32_e32 v169, s18, v5
	v_med3_i32 v169, v169, 0, s17
	v_lshl_add_u32 v169, v169, s16, v6
	global_load_dwordx4 v[148:151], v169, s[10:11] offset:1024
	global_load_dwordx4 v[152:155], v169, s[10:11] offset:1056
	global_load_dwordx4 v[156:159], v169, s[10:11] offset:1088
	global_load_dwordx4 v[160:163], v169, s[10:11] offset:1120
	v_bfe_u32 v171, v7, s28, 8
	v_lshl_add_u32 v171, v171, 4, s27
	s_mov_b64 exec, s[42:43]
	global_load_dword v164, v171, s[4:5]
	s_mov_b64 exec, -1
